# index: cache-warming prefetch of the next task's 4 query rows (qi slice of PROJ + SMALL rows) issued at the start of the current task's scoring loop
# baseline (speedup 1.0000x reference)
.Lq_pre:
	v_readlane_b32 s42, v254, 40
	v_readlane_b32 s43, v254, 41
	s_add_i32 s29, s59, 1
	s_bitcmp0_b32 s29, 0
	s_cselect_b32 s30, s2, s52
	s_mul_i32 s29, s29, s49
	s_add_i32 s29, s29, s30
	s_cmpk_gt_i32 s29, 0xfff
	s_cbranch_scc1 .Lq_nowarm
	s_lshl_b32 s29, s29, 2
	s_sub_i32 s29, 0x3ffc, s29
	s_movk_i32 s31, 0x2200
	v_bfe_u32 v223, v114, 4, 2
	v_add_u32_e32 v223, s29, v223
	v_and_b32_e32 v222, 15, v114
	v_lshlrev_b32_e32 v222, 7, v222
	v_mad_u32_u24 v224, v223, s31, v222
	v_add_u32_e32 v224, 0x24a01800, v224
	global_load_dword v226, v224, s[42:43]
	v_and_b32_e32 v222, 0x180, v222
	v_lshl_add_u32 v225, v223, 9, v222
	v_add_u32_e32 v225, 0x31200000, v225
	global_load_dword v227, v225, s[42:43]
.Lq_nowarm:
	s_mov_b32 s63, 0x20000
	s_mov_b32 s64, 0x8000
	v_readlane_b32 s65, v253, 0
	s_cmp_lt_u32 s65, 4
	s_cbranch_scc1 .Lq_noprio
	s_setprio 1
